# speedup vs baseline: 1.0231x; 1.0086x over previous
.LBB6_37:
	ds_bpermute_b32 v33, v165, v38
	s_mov_b32 s6, 0x42800000
	s_add_u32 s0, s34, s26
	s_addc_u32 s1, s33, 0
	s_lshl_b64 s[0:1], s[0:1], 13
	s_waitcnt lgkmcnt(0)
	v_add_f32_e32 v33, v38, v33
	v_div_scale_f32 v34, s[4:5], v33, v33, s6
	v_rcp_f32_e32 v35, v34
	v_div_scale_f32 v36, vcc, s6, v33, s6
	s_cmp_lt_u32 s29, 64
	v_fma_f32 v37, -v34, v35, 1.0
	v_fmac_f32_e32 v35, v37, v35
	v_mul_f32_e32 v37, v36, v35
	v_fma_f32 v38, -v34, v37, v36
	v_fmac_f32_e32 v37, v38, v35
	v_fma_f32 v34, -v34, v37, v36
	v_div_fmas_f32 v34, v34, v35, v37
	v_div_fixup_f32 v33, v34, v33, s6
	v_mul_f32_e32 v16, v16, v33
	v_mul_f32_e32 v34, v17, v33
	v_mul_f32_e32 v35, v18, v33
	v_mov_b32_e32 v18, 0
	v_mul_f32_e32 v36, v19, v33
	v_cvt_pk_fp8_f32 v18, v16, v34
	v_mul_f32_e32 v16, v20, v33
	v_mul_f32_e32 v20, v21, v33
	v_mov_b32_e32 v19, 0
	v_cvt_pk_fp8_f32 v19, v16, v20
	v_mul_f32_e32 v16, v22, v33
	v_mul_f32_e32 v20, v23, v33
	v_mul_f32_e32 v21, v25, v33
	v_cvt_pk_fp8_f32 v19, v16, v20 op_sel:[0,0,1]
	v_mul_f32_e32 v16, v24, v33
	v_mov_b32_e32 v20, 0
	v_cvt_pk_fp8_f32 v20, v16, v21
	v_mul_f32_e32 v16, v28, v33
	v_mul_f32_e32 v24, v29, v33
	v_mov_b32_e32 v21, 0
	v_cvt_pk_fp8_f32 v21, v16, v24
	ds_bpermute_b32 v16, v165, v32
	v_mul_f32_e32 v22, v26, v33
	v_mul_f32_e32 v23, v27, v33
	v_cvt_pk_fp8_f32 v20, v22, v23 op_sel:[0,0,1]
	v_mul_f32_e32 v22, v30, v33
	s_waitcnt lgkmcnt(0)
	v_add_f32_e32 v16, v32, v16
	v_mul_f32_e32 v23, v31, v33
	v_div_scale_f32 v24, s[4:5], v16, v16, s6
	v_cvt_pk_fp8_f32 v18, v35, v36 op_sel:[0,0,1]
	v_cvt_pk_fp8_f32 v21, v22, v23 op_sel:[0,0,1]
	v_rcp_f32_e32 v25, v24
	v_lshl_add_u64 v[22:23], v[150:151], 0, s[0:1]
	s_movk_i32 s0, 0x2000
	global_store_dwordx4 v[22:23], v[18:21], off sc1
	v_mov_b32_e32 v17, 0
	s_nop 0
	v_fma_f32 v18, -v24, v25, 1.0
	v_fmac_f32_e32 v25, v18, v25
	v_div_scale_f32 v18, vcc, s6, v16, s6
	v_mul_f32_e32 v19, v18, v25
	v_fma_f32 v20, -v24, v19, v18
	v_fmac_f32_e32 v19, v20, v25
	v_fma_f32 v18, -v24, v19, v18
	v_div_fmas_f32 v18, v18, v25, v19
	v_div_fixup_f32 v16, v18, v16, s6
	v_mul_f32_e32 v18, v0, v16
	v_mul_f32_e32 v1, v1, v16
	v_mov_b32_e32 v0, 0
	v_cvt_pk_fp8_f32 v0, v18, v1
	v_mul_f32_e32 v4, v4, v16
	v_mul_f32_e32 v5, v5, v16
	v_mov_b32_e32 v1, 0
	v_cvt_pk_fp8_f32 v1, v4, v5
	v_mul_f32_e32 v2, v2, v16
	v_mul_f32_e32 v3, v3, v16
	v_cvt_pk_fp8_f32 v0, v2, v3 op_sel:[0,0,1]
	v_mul_f32_e32 v2, v6, v16
	v_mul_f32_e32 v3, v7, v16
	v_cvt_pk_fp8_f32 v1, v2, v3 op_sel:[0,0,1]
	v_mul_f32_e32 v3, v8, v16
	v_mul_f32_e32 v4, v9, v16
	v_mov_b32_e32 v2, 0
	v_cvt_pk_fp8_f32 v2, v3, v4
	v_mul_f32_e32 v4, v12, v16
	v_mul_f32_e32 v7, v13, v16
	v_mov_b32_e32 v3, 0
	v_cvt_pk_fp8_f32 v3, v4, v7
	v_mul_f32_e32 v5, v10, v16
	v_mul_f32_e32 v6, v11, v16
	v_cvt_pk_fp8_f32 v2, v5, v6 op_sel:[0,0,1]
	v_mul_f32_e32 v4, v14, v16
	v_mul_f32_e32 v5, v15, v16
	v_cvt_pk_fp8_f32 v3, v4, v5 op_sel:[0,0,1]
	v_add_co_u32_e32 v4, vcc, s0, v22
	s_cselect_b64 s[0:1], -1, 0
	s_nop 0
	v_addc_co_u32_e32 v5, vcc, 0, v23, vcc
	s_and_b64 s[0:1], s[2:3], s[0:1]
	global_store_dwordx4 v[4:5], v[0:3], off sc1
	s_barrier
	s_cmp_eq_u64 s[0:1], 0
	s_cbranch_scc1 .LBB6_39
	v_mbcnt_lo_u32_b32 v0, -1, 0
	v_mbcnt_hi_u32_b32 v0, -1, v0
	v_lshrrev_b32_e32 v1, 4, v0
	v_and_b32_e32 v2, 15, v0
	v_mul_u32_u24_e32 v3, 0x50, v1
	v_add_u32_e32 v3, 0x21000, v3
	v_lshl_add_u32 v4, v2, 2, v3
	ds_read_b64 v[10:11], v3
	ds_read_b64 v[12:13], v3 offset:320
	ds_read_b64 v[14:15], v3 offset:640
	ds_read_b64 v[16:17], v3 offset:960
	ds_read_b64 v[18:19], v3 offset:1280
	ds_read_b64 v[20:21], v3 offset:1600
	ds_read_b64 v[22:23], v3 offset:1920
	ds_read_b64 v[24:25], v3 offset:2240
	ds_read_b32 v30, v4 offset:8
	ds_read_b32 v31, v4 offset:328
	ds_read_b32 v32, v4 offset:648
	ds_read_b32 v33, v4 offset:968
	ds_read_b32 v34, v4 offset:1288
	ds_read_b32 v35, v4 offset:1608
	ds_read_b32 v36, v4 offset:1928
	ds_read_b32 v37, v4 offset:2248
	s_mul_i32 s0, s30, 0x108
	s_mul_hi_i32 s1, s30, 0x108
	s_or_b32 s0, s0, s28
	s_lshl_b64 s[0:1], s[0:1], 11
	s_add_u32 s0, s24, s0
	s_addc_u32 s1, s25, s1
	s_add_u32 s0, s0, 0x80000
	s_addc_u32 s1, s1, 0
	v_and_b32_e32 v9, 1, v1
	v_lshrrev_b32_e32 v51, 1, v1
	v_lshl_or_b32 v9, v51, 5, v9
	v_lshrrev_b32_e32 v51, 3, v2
	v_and_b32_e32 v52, 7, v2
	v_lshlrev_b32_e32 v9, 3, v9
	v_lshl_or_b32 v9, v51, 9, v9
	v_or_b32_e32 v9, v9, v52
	v_lshlrev_b32_e32 v9, 1, v9
	s_waitcnt lgkmcnt(0)
	v_max3_f32 v5, v10, v12, v14
	v_max3_f32 v5, v5, v16, v18
	v_max3_f32 v5, v5, v20, v22
	v_max_f32_e32 v5, v5, v24
	v_sub_f32_e32 v40, v10, v5
	v_sub_f32_e32 v41, v12, v5
	v_sub_f32_e32 v42, v14, v5
	v_sub_f32_e32 v43, v16, v5
	v_sub_f32_e32 v44, v18, v5
	v_sub_f32_e32 v45, v20, v5
	v_sub_f32_e32 v46, v22, v5
	v_sub_f32_e32 v47, v24, v5
	v_exp_f32_e32 v40, v40
	v_exp_f32_e32 v41, v41
	v_exp_f32_e32 v42, v42
	v_exp_f32_e32 v43, v43
	v_exp_f32_e32 v44, v44
	v_exp_f32_e32 v45, v45
	v_exp_f32_e32 v46, v46
	v_exp_f32_e32 v47, v47
	s_nop 0
	v_mul_f32_e32 v6, v11, v40
	v_mul_f32_e32 v7, v30, v40
	v_fmac_f32_e32 v6, v13, v41
	v_fmac_f32_e32 v7, v31, v41
	v_fmac_f32_e32 v6, v15, v42
	v_fmac_f32_e32 v7, v32, v42
	v_fmac_f32_e32 v6, v17, v43
	v_fmac_f32_e32 v7, v33, v43
	v_fmac_f32_e32 v6, v19, v44
	v_fmac_f32_e32 v7, v34, v44
	v_fmac_f32_e32 v6, v21, v45
	v_fmac_f32_e32 v7, v35, v45
	v_fmac_f32_e32 v6, v23, v46
	v_fmac_f32_e32 v7, v36, v46
	v_fmac_f32_e32 v6, v25, v47
	v_fmac_f32_e32 v7, v37, v47
	v_div_scale_f32 v60, s[2:3], v6, v6, v7
	v_rcp_f32_e32 v61, v60
	s_nop 0
	v_fma_f32 v62, -v60, v61, 1.0
	v_fmac_f32_e32 v61, v62, v61
	v_div_scale_f32 v62, vcc, v7, v6, v7
	v_mul_f32_e32 v63, v62, v61
	v_fma_f32 v64, -v60, v63, v62
	v_fmac_f32_e32 v63, v64, v61
	v_fma_f32 v60, -v60, v63, v62
	v_div_fmas_f32 v60, v60, v61, v63
	v_div_fixup_f32 v8, v60, v6, v7
	v_cvt_pk_bf16_f32 v8, v8, v8
	global_store_short v9, v8, s[0:1]
